# speedup vs baseline: 1.0487x; 1.0057x over previous
.Llight_path:
	s_waitcnt vmcnt(0)
	v_mul_u32_u24_e32 v236, 36, v228
	v_add_u32_e32 v236, v236, v230
	v_add_u32_e32 v237, s7, v229
	v_mul_u32_u24_e32 v238, 0x104, v228
	v_add_u32_e32 v238, v238, v237
	v_add_u32_e32 v238, 0xb840, v238
	ds_read_b128 v[2:5], v237 offset:36928
	ds_read_b128 v[6:9], v237 offset:36944
	ds_read_b128 v[10:13], v237 offset:36960
	ds_read_b128 v[14:17], v237 offset:36976
	ds_read_b128 v[18:21], v237 offset:37056
	ds_read_b128 v[22:25], v237 offset:37072
	ds_read_b128 v[26:29], v237 offset:37088
	ds_read_b128 v[30:33], v237 offset:37104
	ds_read_b128 v[162:165], v236 offset:16384
	ds_read_b128 v[166:169], v236 offset:16416
	ds_read_b128 v[170:173], v236 offset:16448
	ds_read_b128 v[174:177], v236 offset:16480
	s_waitcnt lgkmcnt(0)
	v_mfma_f32_32x32x16_bf16 v[2:17], v[94:97], v[162:165], v[2:17]
	v_mfma_f32_32x32x16_bf16 v[2:17], v[90:93], v[166:169], v[2:17]
	v_mfma_f32_32x32x16_bf16 v[2:17], v[86:89], v[170:173], v[2:17]
	v_mfma_f32_32x32x16_bf16 v[2:17], v[82:85], v[174:177], v[2:17]
	v_mfma_f32_32x32x16_bf16 v[18:33], v[46:49], v[162:165], v[18:33]
	ds_read_b128 v[130:133], v237 offset:36928
	ds_read_b128 v[134:137], v237 offset:36944
	ds_read_b128 v[138:141], v237 offset:36960
	v_mfma_f32_32x32x16_bf16 v[18:33], v[42:45], v[166:169], v[18:33]
	ds_read_b128 v[142:145], v237 offset:36976
	ds_read_b128 v[146:149], v237 offset:37056
	ds_read_b128 v[150:153], v237 offset:37072
	v_mfma_f32_32x32x16_bf16 v[18:33], v[38:41], v[170:173], v[18:33]
	ds_read_b128 v[154:157], v237 offset:37088
	ds_read_b128 v[158:161], v237 offset:37104
	ds_read_b128 v[178:181], v236 offset:20992
	v_mfma_f32_32x32x16_bf16 v[18:33], v[34:37], v[174:177], v[18:33]
	ds_read_b128 v[182:185], v236 offset:21024
	ds_read_b128 v[186:189], v236 offset:21056
	ds_read_b128 v[190:193], v236 offset:21088
	s_waitcnt lgkmcnt(0)
	v_mfma_f32_32x32x16_bf16 v[130:145], v[94:97], v[178:181], v[130:145]
	v_mfma_f32_32x32x16_bf16 v[130:145], v[90:93], v[182:185], v[130:145]
	v_mfma_f32_32x32x16_bf16 v[130:145], v[86:89], v[186:189], v[130:145]
	v_mfma_f32_32x32x16_bf16 v[130:145], v[82:85], v[190:193], v[130:145]
	s_nop 7
	ds_write_b128 v238, v[2:5] offset:0
	ds_write_b128 v238, v[6:9] offset:16
	ds_write_b128 v238, v[10:13] offset:32
	ds_write_b128 v238, v[14:17] offset:48
	ds_write_b128 v238, v[18:21] offset:128
	ds_write_b128 v238, v[22:25] offset:144
	ds_write_b128 v238, v[26:29] offset:160
	ds_write_b128 v238, v[30:33] offset:176
	v_mfma_f32_32x32x16_bf16 v[146:161], v[46:49], v[178:181], v[146:161]
	ds_read_b128 v[2:5], v237 offset:36928
	ds_read_b128 v[6:9], v237 offset:36944
	ds_read_b128 v[10:13], v237 offset:36960
	v_mfma_f32_32x32x16_bf16 v[146:161], v[42:45], v[182:185], v[146:161]
	ds_read_b128 v[14:17], v237 offset:36976
	ds_read_b128 v[18:21], v237 offset:37056
	ds_read_b128 v[22:25], v237 offset:37072
	v_mfma_f32_32x32x16_bf16 v[146:161], v[38:41], v[186:189], v[146:161]
	ds_read_b128 v[26:29], v237 offset:37088
	ds_read_b128 v[30:33], v237 offset:37104
	ds_read_b128 v[162:165], v236 offset:25600
	v_mfma_f32_32x32x16_bf16 v[146:161], v[34:37], v[190:193], v[146:161]
	ds_read_b128 v[166:169], v236 offset:25632
	ds_read_b128 v[170:173], v236 offset:25664
	ds_read_b128 v[174:177], v236 offset:25696
	s_waitcnt lgkmcnt(0)
	v_mfma_f32_32x32x16_bf16 v[2:17], v[94:97], v[162:165], v[2:17]
	v_mfma_f32_32x32x16_bf16 v[2:17], v[90:93], v[166:169], v[2:17]
	v_mfma_f32_32x32x16_bf16 v[2:17], v[86:89], v[170:173], v[2:17]
	v_mfma_f32_32x32x16_bf16 v[2:17], v[82:85], v[174:177], v[2:17]
	s_nop 7
	v_add_u32_e32 v239, 0x8200, v238
	ds_write_b128 v239, v[130:133] offset:0
	ds_write_b128 v239, v[134:137] offset:16
	ds_write_b128 v239, v[138:141] offset:32
	ds_write_b128 v239, v[142:145] offset:48
	ds_write_b128 v239, v[146:149] offset:128
	ds_write_b128 v239, v[150:153] offset:144
	ds_write_b128 v239, v[154:157] offset:160
	ds_write_b128 v239, v[158:161] offset:176
	v_mfma_f32_32x32x16_bf16 v[18:33], v[46:49], v[162:165], v[18:33]
	ds_read_b128 v[130:133], v237 offset:36928
	ds_read_b128 v[134:137], v237 offset:36944
	ds_read_b128 v[138:141], v237 offset:36960
	v_mfma_f32_32x32x16_bf16 v[18:33], v[42:45], v[166:169], v[18:33]
	ds_read_b128 v[142:145], v237 offset:36976
	ds_read_b128 v[146:149], v237 offset:37056
	ds_read_b128 v[150:153], v237 offset:37072
	v_mfma_f32_32x32x16_bf16 v[18:33], v[38:41], v[170:173], v[18:33]
	ds_read_b128 v[154:157], v237 offset:37088
	ds_read_b128 v[158:161], v237 offset:37104
	ds_read_b128 v[178:181], v236 offset:30208
	v_mfma_f32_32x32x16_bf16 v[18:33], v[34:37], v[174:177], v[18:33]
	ds_read_b128 v[182:185], v236 offset:30240
	ds_read_b128 v[186:189], v236 offset:30272
	ds_read_b128 v[190:193], v236 offset:30304
	s_waitcnt lgkmcnt(0)
	v_mfma_f32_32x32x16_bf16 v[130:145], v[94:97], v[178:181], v[130:145]
	v_mfma_f32_32x32x16_bf16 v[130:145], v[90:93], v[182:185], v[130:145]
	v_mfma_f32_32x32x16_bf16 v[130:145], v[86:89], v[186:189], v[130:145]
	v_mfma_f32_32x32x16_bf16 v[130:145], v[82:85], v[190:193], v[130:145]
	s_nop 7
	v_add_u32_e32 v239, 0x10400, v238
	ds_write_b128 v239, v[2:5] offset:0
	ds_write_b128 v239, v[6:9] offset:16
	ds_write_b128 v239, v[10:13] offset:32
	ds_write_b128 v239, v[14:17] offset:48
	ds_write_b128 v239, v[18:21] offset:128
	ds_write_b128 v239, v[22:25] offset:144
	ds_write_b128 v239, v[26:29] offset:160
	ds_write_b128 v239, v[30:33] offset:176
	v_mfma_f32_32x32x16_bf16 v[146:161], v[46:49], v[178:181], v[146:161]
	v_mfma_f32_32x32x16_bf16 v[146:161], v[42:45], v[182:185], v[146:161]
	v_mfma_f32_32x32x16_bf16 v[146:161], v[38:41], v[186:189], v[146:161]
	v_mfma_f32_32x32x16_bf16 v[146:161], v[34:37], v[190:193], v[146:161]
	s_nop 7
	s_nop 7
	v_cmp_gt_u32_e32 vcc, 16, v228
	s_and_saveexec_b64 s[20:21], vcc
	v_add_u32_e32 v239, 0x18600, v238
	ds_write_b128 v239, v[130:133] offset:0
	ds_write_b128 v239, v[134:137] offset:16
	ds_write_b128 v239, v[138:141] offset:32
	ds_write_b128 v239, v[142:145] offset:48
	ds_write_b128 v239, v[146:149] offset:128
	ds_write_b128 v239, v[150:153] offset:144
	ds_write_b128 v239, v[154:157] offset:160
	ds_write_b128 v239, v[158:161] offset:176
	s_or_b64 exec, exec, s[20:21]
	s_waitcnt lgkmcnt(0)
	s_nop 7
	s_nop 7
	v_add_u32_e32 v231, s7, v229
	v_add_u32_e32 v231, 0xb840, v231
	v_add_u32_e32 v211, s6, v210
	s_mov_b32 s12, 0x4038aa3b
	v_mov_b32_e32 v235, 0xc038aa3b
	s_nop 0
	s_load_dwordx8 s[4:11], s[0:1], 0x10
	s_waitcnt lgkmcnt(0)
	v_add_u32_e32 v232, 0x24e80, v228
	ds_read_b32 v244, v232
	ds_read_b32 v245, v232 offset:128
	v_mov_b32_e32 v194, 0
	v_mov_b32_e32 v195, 0
	v_mov_b32_e32 v196, 0
	v_mov_b32_e32 v197, 0
	v_mov_b32_e32 v198, 0
	v_mov_b32_e32 v199, 0
	v_mov_b32_e32 v200, 0
	v_mov_b32_e32 v201, 0
	v_mov_b32_e32 v202, 0
	v_mov_b32_e32 v203, 0
	v_mov_b32_e32 v204, 0
	v_mov_b32_e32 v205, 0
	v_mov_b32_e32 v206, 0
	v_mov_b32_e32 v207, 0
	v_mov_b32_e32 v208, 0
	v_mov_b32_e32 v209, 0
	v_add_u32_e32 v232, 0x100, v232
	s_waitcnt lgkmcnt(0)
	v_add_u32_e32 v233, v231, v244
	v_add_u32_e32 v234, v231, v245
	ds_read_b128 v[2:5], v233 offset:0
	ds_read_b128 v[6:9], v233 offset:16
	ds_read_b128 v[10:13], v233 offset:32
	ds_read_b128 v[14:17], v233 offset:48
	ds_read_b128 v[18:21], v233 offset:128
	ds_read_b128 v[22:25], v233 offset:144
	ds_read_b128 v[26:29], v233 offset:160
	ds_read_b128 v[30:33], v233 offset:176
	ds_read_b128 v[34:37], v234 offset:0
	ds_read_b128 v[38:41], v234 offset:16
	ds_read_b128 v[42:45], v234 offset:32
	ds_read_b128 v[46:49], v234 offset:48
	s_movk_i32 s16, 18
	s_waitcnt lgkmcnt(0)
	ds_read_b128 v[82:85], v234 offset:128
	ds_read_b128 v[86:89], v234 offset:144
	ds_read_b128 v[90:93], v234 offset:160
	ds_read_b128 v[94:97], v234 offset:176
	ds_read_b32 v244, v232 offset:0
	v_exp_f32_e32 v212, v4
	v_exp_f32_e32 v213, v8
	v_exp_f32_e32 v214, v12
	v_exp_f32_e32 v215, v16
	v_exp_f32_e32 v216, v2
	v_exp_f32_e32 v217, v6
	v_exp_f32_e32 v218, v10
	v_exp_f32_e32 v219, v14
	v_add_f32_e32 v236, 1.0, v212
	v_add_f32_e32 v237, 1.0, v213
	v_add_f32_e32 v238, 1.0, v214
	v_add_f32_e32 v239, 1.0, v215
	v_fma_f32 v240, v212, s12, v235
	v_fma_f32 v241, v213, s12, v235
	v_fma_f32 v242, v214, s12, v235
	v_fma_f32 v243, v215, s12, v235
	v_fmac_f32_e32 v236, v216, v236
	v_fmac_f32_e32 v237, v217, v237
	v_fmac_f32_e32 v238, v218, v238
	v_fmac_f32_e32 v239, v219, v239
	v_rcp_f32_e32 v216, v236
	v_rcp_f32_e32 v217, v237
	v_rcp_f32_e32 v218, v238
	v_rcp_f32_e32 v219, v239
	v_exp_f32_e32 v224, v5
	v_exp_f32_e32 v225, v9
	v_exp_f32_e32 v226, v13
	v_exp_f32_e32 v227, v17
	v_mul_f32_e32 v194, v240, v216
	v_mul_f32_e32 v195, v241, v217
	v_mul_f32_e32 v196, v242, v218
	v_mul_f32_e32 v197, v243, v219
	v_exp_f32_e32 v212, v194
	v_exp_f32_e32 v213, v195
	v_exp_f32_e32 v214, v196
	v_exp_f32_e32 v215, v197
	v_add_f32_e32 v224, 1.0, v224
	v_add_f32_e32 v225, 1.0, v225
	v_add_f32_e32 v226, 1.0, v226
	v_add_f32_e32 v227, 1.0, v227
	v_fmac_f32_e32 v224, v224, v212
	v_fmac_f32_e32 v225, v225, v213
	v_fmac_f32_e32 v226, v226, v214
	v_fmac_f32_e32 v227, v227, v215
	v_rcp_f32_e32 v224, v224
	v_rcp_f32_e32 v225, v225
	v_rcp_f32_e32 v226, v226
	v_rcp_f32_e32 v227, v227
	v_fma_f32 v224, -v212, v224, v224
	v_fma_f32 v225, -v213, v225, v225
	v_fma_f32 v226, -v214, v226, v226
	v_fma_f32 v227, -v215, v227, v227
	v_cvt_pk_bf16_f32 v224, v224, v225
	v_cvt_pk_bf16_f32 v225, v226, v227
	ds_write_b64 v211, v[224:225] offset:0
	s_waitcnt lgkmcnt(1)
	v_add_u32_e32 v233, v231, v244
	ds_read_b128 v[2:5], v233 offset:0
	ds_read_b128 v[6:9], v233 offset:16
	ds_read_b128 v[10:13], v233 offset:32
	ds_read_b128 v[14:17], v233 offset:48
	v_exp_f32_e32 v212, v20
	v_exp_f32_e32 v213, v24
	v_exp_f32_e32 v214, v28
	v_exp_f32_e32 v215, v32
	v_exp_f32_e32 v216, v18
	v_exp_f32_e32 v217, v22
	v_exp_f32_e32 v218, v26
	v_exp_f32_e32 v219, v30
	v_add_f32_e32 v236, 1.0, v212
	v_add_f32_e32 v237, 1.0, v213
	v_add_f32_e32 v238, 1.0, v214
	v_add_f32_e32 v239, 1.0, v215
	v_fma_f32 v240, v212, s12, v235
	v_fma_f32 v241, v213, s12, v235
	v_fma_f32 v242, v214, s12, v235
	v_fma_f32 v243, v215, s12, v235
	v_fmac_f32_e32 v236, v216, v236
	v_fmac_f32_e32 v237, v217, v237
	v_fmac_f32_e32 v238, v218, v238
	v_fmac_f32_e32 v239, v219, v239
	v_rcp_f32_e32 v216, v236
	v_rcp_f32_e32 v217, v237
	v_rcp_f32_e32 v218, v238
	v_rcp_f32_e32 v219, v239
	v_exp_f32_e32 v224, v21
	v_exp_f32_e32 v225, v25
	v_exp_f32_e32 v226, v29
	v_exp_f32_e32 v227, v33
	v_mul_f32_e32 v198, v240, v216
	v_mul_f32_e32 v199, v241, v217
	v_mul_f32_e32 v200, v242, v218
	v_mul_f32_e32 v201, v243, v219
	v_exp_f32_e32 v212, v198
	v_exp_f32_e32 v213, v199
	v_exp_f32_e32 v214, v200
	v_exp_f32_e32 v215, v201
	v_add_f32_e32 v224, 1.0, v224
	v_add_f32_e32 v225, 1.0, v225
	v_add_f32_e32 v226, 1.0, v226
	v_add_f32_e32 v227, 1.0, v227
	v_fmac_f32_e32 v224, v224, v212
	v_fmac_f32_e32 v225, v225, v213
	v_fmac_f32_e32 v226, v226, v214
	v_fmac_f32_e32 v227, v227, v215
	v_rcp_f32_e32 v224, v224
	v_rcp_f32_e32 v225, v225
	v_rcp_f32_e32 v226, v226
	v_rcp_f32_e32 v227, v227
	v_fma_f32 v224, -v212, v224, v224
	v_fma_f32 v225, -v213, v225, v225
	v_fma_f32 v226, -v214, v226, v226
	v_fma_f32 v227, -v215, v227, v227
	v_cvt_pk_bf16_f32 v224, v224, v225
	v_cvt_pk_bf16_f32 v225, v226, v227
	ds_write_b64 v211, v[224:225] offset:8
	s_waitcnt lgkmcnt(0)
	s_barrier
	ds_read_b128 v[130:133], v210 offset:0
	ds_read_b128 v[134:137], v210 offset:1024
	ds_read_b128 v[18:21], v233 offset:128
	ds_read_b128 v[22:25], v233 offset:144
	ds_read_b128 v[26:29], v233 offset:160
	ds_read_b128 v[30:33], v233 offset:176
	ds_read_b32 v245, v232 offset:128
	v_exp_f32_e32 v212, v36
	v_exp_f32_e32 v213, v40
	v_exp_f32_e32 v214, v44
	v_exp_f32_e32 v215, v48
	ds_read_b128 v[138:141], v210 offset:2048
	ds_read_b128 v[142:145], v210 offset:3072
	v_exp_f32_e32 v216, v34
	v_exp_f32_e32 v217, v38
	v_exp_f32_e32 v218, v42
	v_exp_f32_e32 v219, v46
	v_add_f32_e32 v236, 1.0, v212
	v_add_f32_e32 v237, 1.0, v213
	v_add_f32_e32 v238, 1.0, v214
	v_add_f32_e32 v239, 1.0, v215
	v_fma_f32 v240, v212, s12, v235
	v_fma_f32 v241, v213, s12, v235
	v_fma_f32 v242, v214, s12, v235
	v_fma_f32 v243, v215, s12, v235
	ds_read_b128 v[146:149], v210 offset:4096
	ds_read_b128 v[150:153], v210 offset:5120
	v_fmac_f32_e32 v236, v216, v236
	v_fmac_f32_e32 v237, v217, v237
	v_fmac_f32_e32 v238, v218, v238
	v_fmac_f32_e32 v239, v219, v239
	ds_read_b128 v[154:157], v210 offset:6144
	ds_read_b128 v[158:161], v210 offset:7168
	v_rcp_f32_e32 v216, v236
	v_rcp_f32_e32 v217, v237
	v_rcp_f32_e32 v218, v238
	v_rcp_f32_e32 v219, v239
	v_exp_f32_e32 v224, v37
	v_exp_f32_e32 v225, v41
	v_exp_f32_e32 v226, v45
	v_exp_f32_e32 v227, v49
	v_mul_f32_e32 v202, v240, v216
	v_mul_f32_e32 v203, v241, v217
	v_mul_f32_e32 v204, v242, v218
	v_mul_f32_e32 v205, v243, v219
	v_exp_f32_e32 v212, v202
	v_exp_f32_e32 v213, v203
	v_exp_f32_e32 v214, v204
	v_exp_f32_e32 v215, v205
	v_add_f32_e32 v224, 1.0, v224
	v_add_f32_e32 v225, 1.0, v225
	v_add_f32_e32 v226, 1.0, v226
	v_add_f32_e32 v227, 1.0, v227
	v_fmac_f32_e32 v224, v224, v212
	v_fmac_f32_e32 v225, v225, v213
	v_fmac_f32_e32 v226, v226, v214
	v_fmac_f32_e32 v227, v227, v215
	v_rcp_f32_e32 v224, v224
	v_rcp_f32_e32 v225, v225
	v_rcp_f32_e32 v226, v226
	v_rcp_f32_e32 v227, v227
	v_fma_f32 v224, -v212, v224, v224
	v_fma_f32 v225, -v213, v225, v225
	v_fma_f32 v226, -v214, v226, v226
	v_fma_f32 v227, -v215, v227, v227
	v_cvt_pk_bf16_f32 v224, v224, v225
	v_cvt_pk_bf16_f32 v225, v226, v227
	ds_write_b64 v211, v[224:225] offset:8192
	s_waitcnt lgkmcnt(1)
	v_mfma_f32_32x32x16_bf16 v[2:17], v[126:129], v[130:133], v[2:17]
	v_add_u32_e32 v234, v231, v245
	ds_read_b128 v[34:37], v234 offset:0
	ds_read_b128 v[38:41], v234 offset:16
	ds_read_b128 v[42:45], v234 offset:32
	ds_read_b128 v[46:49], v234 offset:48
	v_add_u32_e32 v232, 0x100, v232
	v_exp_f32_e32 v212, v84
	v_exp_f32_e32 v213, v88
	v_exp_f32_e32 v214, v92
	v_exp_f32_e32 v215, v96
	v_mfma_f32_32x32x16_bf16 v[2:17], v[122:125], v[134:137], v[2:17]
	v_exp_f32_e32 v216, v82
	v_exp_f32_e32 v217, v86
	v_exp_f32_e32 v218, v90
	v_exp_f32_e32 v219, v94
	v_add_f32_e32 v236, 1.0, v212
	v_add_f32_e32 v237, 1.0, v213
	v_add_f32_e32 v238, 1.0, v214
	v_add_f32_e32 v239, 1.0, v215
	v_fma_f32 v240, v212, s12, v235
	v_fma_f32 v241, v213, s12, v235
	v_fma_f32 v242, v214, s12, v235
	v_fma_f32 v243, v215, s12, v235
	v_mfma_f32_32x32x16_bf16 v[2:17], v[118:121], v[138:141], v[2:17]
	v_fmac_f32_e32 v236, v216, v236
	v_fmac_f32_e32 v237, v217, v237
	v_fmac_f32_e32 v238, v218, v238
	v_fmac_f32_e32 v239, v219, v239
	v_mfma_f32_32x32x16_bf16 v[2:17], v[114:117], v[142:145], v[2:17]
	v_rcp_f32_e32 v216, v236
	v_rcp_f32_e32 v217, v237
	v_rcp_f32_e32 v218, v238
	v_rcp_f32_e32 v219, v239
	v_mfma_f32_32x32x16_bf16 v[2:17], v[110:113], v[146:149], v[2:17]
	v_exp_f32_e32 v224, v85
	v_exp_f32_e32 v225, v89
	v_exp_f32_e32 v226, v93
	v_exp_f32_e32 v227, v97
	v_mul_f32_e32 v206, v240, v216
	v_mul_f32_e32 v207, v241, v217
	v_mul_f32_e32 v208, v242, v218
	v_mul_f32_e32 v209, v243, v219
	v_mfma_f32_32x32x16_bf16 v[2:17], v[106:109], v[150:153], v[2:17]
	v_mfma_f32_32x32x16_bf16 v[2:17], v[102:105], v[154:157], v[2:17]
	v_exp_f32_e32 v212, v206
	v_exp_f32_e32 v213, v207
	v_exp_f32_e32 v214, v208
	v_exp_f32_e32 v215, v209
	v_add_f32_e32 v224, 1.0, v224
	v_add_f32_e32 v225, 1.0, v225
	v_add_f32_e32 v226, 1.0, v226
	v_add_f32_e32 v227, 1.0, v227
	v_fmac_f32_e32 v224, v224, v212
	v_fmac_f32_e32 v225, v225, v213
	v_fmac_f32_e32 v226, v226, v214
	v_fmac_f32_e32 v227, v227, v215
	v_mfma_f32_32x32x16_bf16 v[2:17], v[98:101], v[158:161], v[2:17]
	v_rcp_f32_e32 v224, v224
	v_rcp_f32_e32 v225, v225
	v_rcp_f32_e32 v226, v226
	v_rcp_f32_e32 v227, v227
	v_fma_f32 v224, -v212, v224, v224
	v_fma_f32 v225, -v213, v225, v225
	v_fma_f32 v226, -v214, v226, v226
	v_fma_f32 v227, -v215, v227, v227
	v_cvt_pk_bf16_f32 v224, v224, v225
	v_cvt_pk_bf16_f32 v225, v226, v227
	ds_write_b64 v211, v[224:225] offset:8200
	s_waitcnt lgkmcnt(0)
	s_barrier
